# consolidation: up-GEMM epilogue pad fills + in-proj fp8 epilogue 32-state pads dropped (12 wait states needed, 24+ present), on top of v133
# speedup vs baseline: 1.0025x; 1.0025x over previous
.LBB0_193:
	v_mov_b32_e32 v2, v170
	v_mov_b32_e32 v3, v172
	s_lshl_b32 s7, s66, 8
	s_add_i32 s7, s7, s24
	v_add_u32_e32 v2, s7, v2
	v_lshl_add_u32 v4, v3, 3, s25
	s_lshl_b32 s7, s0, 8
	s_cmp_lt_i32 s0, 8
	s_mov_b64 s[66:67], -1
	v_ashrrev_i32_e32 v5, 31, v4
	v_ashrrev_i32_e32 v3, 31, v2
	s_cbranch_scc1 .LBB0_196
	s_andn2_b64 vcc, exec, s[66:67]
	s_cbranch_vccz .LBB0_197

.LBB0_220:
	v_mov_b32_e32 v2, v166
	v_mov_b32_e32 v3, v167
	s_lshl_b32 s4, s4, 8
	s_add_i32 s4, s4, s24
	v_add_u32_e32 v2, s4, v2
	v_lshl_add_u32 v4, v3, 3, s25
	s_lshl_b32 s4, s76, 8
	s_cmp_lt_i32 s76, 8
	s_mov_b64 s[78:79], -1
	v_ashrrev_i32_e32 v5, 31, v4
	v_ashrrev_i32_e32 v3, 31, v2
	s_cbranch_scc1 .LBB0_223
	s_andn2_b64 vcc, exec, s[78:79]
	s_cbranch_vccz .LBB0_224
